# baseline (speedup 1.0000x reference)
.LBB3_4:
	s_or_b64 exec, exec, s[4:5]
	s_add_i32 s3, 0, 0x20400
	v_mov_b32_e32 v1, s3
	s_waitcnt lgkmcnt(0)
	s_barrier
	ds_read_b64 v[2:3], v1
	v_and_b32_e32 v11, 15, v0
	v_lshrrev_b32_e32 v1, 6, v0
	v_bfe_u32 v14, v0, 4, 2
	v_lshlrev_b32_e32 v12, 2, v1
	s_waitcnt lgkmcnt(0)
	v_readfirstlane_b32 s29, v2
	v_lshlrev_b32_e32 v2, 2, v0
	s_lshl_b32 s30, s29, 4
	v_readfirstlane_b32 s28, v3
	v_lshl_or_b32 v168, s2, 11, v2
	v_or_b32_e32 v2, s30, v11
	v_ashrrev_i32_e32 v3, 31, v2
	s_lshl_b32 s22, s28, 5
	s_ashr_i32 s3, s22, 31
	v_or_b32_e32 v4, v14, v12
	v_lshlrev_b64 v[2:3], 14, v[2:3]
	v_mov_b32_e32 v5, s3
	v_or_b32_e32 v4, s22, v4
	v_lshl_add_u64 v[2:3], s[20:21], 0, v[2:3]
	s_load_dwordx2 s[16:17], s[0:1], 0x0
	v_lshl_add_u64 v[2:3], v[4:5], 4, v[2:3]
	global_load_dwordx4 v[6:9], v[2:3], off
	v_min_u32_e32 v2, 0xbb7ffc, v168
	v_lshlrev_b32_e32 v13, 2, v2
	v_lshl_or_b32 v2, s28, 3, v1
	v_ashrrev_i32_e32 v3, 31, v2
	v_and_b32_e32 v10, 63, v0
	v_lshlrev_b64 v[2:3], 15, v[2:3]
	v_mov_b32_e32 v171, 0
	s_waitcnt lgkmcnt(0)
	v_lshl_add_u64 v[2:3], s[16:17], 0, v[2:3]
	v_lshlrev_b32_e32 v170, 4, v10
	v_lshl_add_u64 v[2:3], v[2:3], 0, v[170:171]
	s_movk_i32 s3, 0x1000
	v_add_co_u32_e32 v4, vcc, s3, v2
	s_movk_i32 s3, 0x2000
	s_nop 0
	v_addc_co_u32_e32 v5, vcc, 0, v3, vcc
	v_add_co_u32_e32 v16, vcc, s3, v2
	s_movk_i32 s3, 0x3000
	s_nop 0
	v_addc_co_u32_e32 v17, vcc, 0, v3, vcc
	v_add_co_u32_e32 v18, vcc, s3, v2
	s_movk_i32 s3, 0x4000
	s_nop 0
	v_addc_co_u32_e32 v19, vcc, 0, v3, vcc
	v_add_co_u32_e32 v20, vcc, s3, v2
	s_movk_i32 s3, 0x5000
	s_nop 0
	v_addc_co_u32_e32 v21, vcc, 0, v3, vcc
	v_add_co_u32_e32 v22, vcc, s3, v2
	s_movk_i32 s3, 0x6000
	s_nop 0
	v_addc_co_u32_e32 v23, vcc, 0, v3, vcc
	v_add_co_u32_e32 v24, vcc, s3, v2
	s_movk_i32 s3, 0x7000
	s_nop 0
	v_addc_co_u32_e32 v25, vcc, 0, v3, vcc
	global_load_dwordx4 v[32:35], v[2:3], off nt
	global_load_dwordx4 v[36:39], v[2:3], off offset:1024 nt
	global_load_dwordx4 v[40:43], v[2:3], off offset:2048 nt
	global_load_dwordx4 v[44:47], v[2:3], off offset:3072 nt
	v_add_co_u32_e32 v2, vcc, s3, v2
	v_cmp_gt_u32_e64 s[6:7], 8, v10
	s_nop 0
	v_addc_co_u32_e32 v3, vcc, 0, v3, vcc
	global_load_dwordx4 v[48:51], v[16:17], off nt
	global_load_dwordx4 v[56:59], v[16:17], off offset:1024 nt
	global_load_dwordx4 v[64:67], v[16:17], off offset:2048 nt
	global_load_dwordx4 v[68:71], v[16:17], off offset:3072 nt
	global_load_dwordx4 v[52:55], v[4:5], off offset:1024 nt
	global_load_dwordx4 v[60:63], v[4:5], off offset:2048 nt
	global_load_dwordx4 v[72:75], v[4:5], off offset:3072 nt
	global_load_dwordx4 v[76:79], v[18:19], off offset:1024 nt
	global_load_dwordx4 v[80:83], v[18:19], off offset:2048 nt
	global_load_dwordx4 v[84:87], v[18:19], off offset:3072 nt
	global_load_dwordx4 v[88:91], v[20:21], off offset:-4096 nt
	global_load_dwordx4 v[92:95], v[20:21], off nt
	global_load_dwordx4 v[96:99], v[20:21], off offset:1024 nt
	global_load_dwordx4 v[100:103], v[20:21], off offset:2048 nt
	global_load_dwordx4 v[104:107], v[20:21], off offset:3072 nt
	global_load_dwordx4 v[108:111], v[24:25], off offset:-4096 nt
	global_load_dwordx4 v[112:115], v[24:25], off nt
	global_load_dwordx4 v[120:123], v[24:25], off offset:1024 nt
	global_load_dwordx4 v[128:131], v[24:25], off offset:2048 nt
	global_load_dwordx4 v[132:135], v[24:25], off offset:3072 nt
	global_load_dwordx4 v[116:119], v[22:23], off offset:1024 nt
	global_load_dwordx4 v[124:127], v[22:23], off offset:2048 nt
	global_load_dwordx4 v[136:139], v[22:23], off offset:3072 nt
	global_load_dwordx4 v[140:143], v[2:3], off nt
	global_load_dwordx4 v[144:147], v[2:3], off offset:1024 nt
	global_load_dwordx4 v[148:151], v[2:3], off offset:2048 nt
	global_load_dwordx4 v[152:155], v[16:17], off offset:-4096 nt
	global_load_dwordx4 v[156:159], v[2:3], off offset:3072 nt
	s_nop 0
	global_load_dwordx4 v[208:211], v13, s[14:15] nt
	v_mbcnt_lo_u32_b32 v13, -1, 0
	v_mbcnt_hi_u32_b32 v18, -1, v13
	v_and_b32_e32 v13, 64, v18
	v_add_u32_e32 v19, 64, v13
	v_xor_b32_e32 v13, 1, v18
	v_cmp_lt_i32_e32 vcc, v13, v19
	v_xor_b32_e32 v15, 2, v18
	v_xor_b32_e32 v20, 4, v18
	v_cndmask_b32_e32 v13, v18, v13, vcc
	v_cmp_lt_i32_e32 vcc, v15, v19
	v_lshlrev_b32_e32 v16, 2, v10
	v_mov_b32_e32 v17, v171
	v_cndmask_b32_e32 v15, v18, v15, vcc
	v_cmp_lt_i32_e32 vcc, v20, v19
	v_lshl_add_u64 v[16:17], s[12:13], 0, v[16:17]
	v_cmp_lt_u32_e64 s[4:5], 7, v10
	v_cndmask_b32_e32 v18, v18, v20, vcc
	v_lshlrev_b32_e32 v13, 2, v13
	v_lshlrev_b32_e32 v15, 2, v15
	v_lshlrev_b32_e32 v18, 2, v18
	s_mov_b32 s3, 0xc3500
